# moe2: LIST and GATE lookups of the next unit issued under the current unit's K loop instead of after it
# speedup vs baseline: 1.0127x; 1.0096x over previous
; __device__ __forceinline__ int moe_row_pidx(const int* pre, const int* LIST, int e, int r) {
;     const int* pf = pre + 1360 + e * NREP;
;     int x = 0;
; #pragma unroll
;     for (int i = 1; i < NREP; ++i) x += (pf[i] <= r);
;     return LIST[((size_t)x * 256 + e) * LCAP + (r - pf[x])];
; }
; __device__ __forceinline__ void moe_local(const int* pre, int* lpre, int x) {
;     if (threadIdx.x == 0) {
;         int s = 0;
;         for (int k = 0; k < 32; ++k) { lpre[k] = s; s += pre[x + 8 * k + 1] - pre[x + 8 * k]; }
;         lpre[32] = s;
;         const int nsh = pre[NE1] - pre[256];
;         lpre[33] = s + (nsh > x ? (nsh - x + 7) / 8 : 0);
;     }
;     __syncthreads();
; }
; __device__ __forceinline__ void moe_unit(const int* pre, const int* lpre, int x, int lb, int& e, int& rb) {
;     if (lb < lpre[32]) {
;         int lo = 0, hi = 32;
;         while (hi - lo > 1) { const int mid = (lo + hi) >> 1; if (lpre[mid] <= lb) lo = mid; else hi = mid; }
;         e = x + 8 * lo; rb = lb - lpre[lo];
;     } else { e = 256; rb = (lb - lpre[32]) * 8 + x; }
; }
.LBB0_1573:
	s_or_b64 exec, exec, s[12:13]
	v_add_co_u32_e32 v2, vcc, 0x60000, v214
	s_nop 1
	v_addc_co_u32_e32 v3, vcc, 0, v215, vcc
	v_add_co_u32_e32 v4, vcc, 0x61000, v214
	s_nop 1
	v_addc_co_u32_e32 v5, vcc, 0, v215, vcc
	global_load_dwordx4 v[118:121], v[2:3], off
	global_load_dwordx4 v[114:117], v[4:5], off
	v_add_co_u32_e32 v2, vcc, 0x62000, v214
	s_nop 1
	v_addc_co_u32_e32 v3, vcc, 0, v215, vcc
	v_add_co_u32_e32 v4, vcc, 0x63000, v214
	s_nop 1
	v_addc_co_u32_e32 v5, vcc, 0, v215, vcc
	global_load_dwordx4 v[130:133], v[2:3], off
	global_load_dwordx4 v[126:129], v[4:5], off
	s_waitcnt lgkmcnt(0)
	s_barrier
	s_add_i32 s64, s23, s27
	v_mov_b64_e32 v[248:249], s[8:9]
	v_mov_b32_e32 v250, -1
	v_mov_b32_e32 v251, 0
	s_cmp_ge_i32 s64, s24
	s_cbranch_scc1 .Lm2a_ld_8
	v_mov_b32_e32 v236, s29
	ds_read_b32 v236, v236
	s_ashr_i32 s65, s64, 2
	s_waitcnt lgkmcnt(0)
	v_cmp_ge_i32_e32 vcc, s65, v236
	s_cbranch_vccz .Lm2a_rt_8
	v_sub_u32_e32 v236, s65, v236
	v_lshlrev_b32_e32 v236, 3, v236
	v_or_b32_e32 v238, s22, v236
	s_movk_i32 s68, 0x100
	s_branch .Lm2a_have_8
.Lm2a_rt_8:
	s_mov_b32 s68, 32
	s_mov_b32 s66, 0
.Lm2a_bs_8:
	s_add_i32 s69, s68, s66
	s_ashr_i32 s69, s69, 1
	s_lshl_b32 s70, s69, 2
	s_add_i32 s70, s70, 0x21890
	v_mov_b32_e32 v236, s70
	ds_read_b32 v236, v236
	s_waitcnt lgkmcnt(0)
	v_readfirstlane_b32 s70, v236
	s_cmp_gt_i32 s70, s65
	s_cselect_b32 s68, s69, s68
	s_cselect_b32 s66, s66, s69
	s_sub_i32 s69, s68, s66
	s_cmp_gt_i32 s69, 1
	s_cbranch_scc1 .Lm2a_bs_8
	s_lshl_b32 s68, s66, 2
	s_add_i32 s68, s68, 0x21890
	v_mov_b32_e32 v236, s68
	ds_read_b32 v236, v236
	s_lshl_b32 s66, s66, 3
	s_or_b32 s68, s66, s22
	s_waitcnt lgkmcnt(0)
	v_sub_u32_e32 v238, s65, v236
.Lm2a_have_8:
	s_lshl_b32 s65, s68, 2
	s_add_i32 s65, s65, 0x20a10
	s_ashr_i32 s69, s68, 31
	s_and_saveexec_b64 s[70:71], s[6:7]
	s_cbranch_execz .Lm2a_x_8
	v_mov_b32_e32 v236, s65
	ds_read_b32 v236, v236 offset:1088
	v_mul_lo_u32 v237, v238, s28
	v_add_u32_e32 v240, v237, v0
	s_waitcnt lgkmcnt(0)
	v_cmp_lt_i32_e32 vcc, v240, v236
	s_and_saveexec_b64 s[72:73], vcc
	s_cbranch_execz .Lm2a_x_8
	s_cmpk_gt_i32 s68, 0xff
	s_cbranch_scc0 .Lm2a_rt2_8
	v_mad_u64_u32 v[236:237], s[74:75], v240, 9, 8
	v_mov_b32_e32 v250, v236
	s_branch .Lm2a_x_8
.Lm2a_rt2_8:
	s_lshl_b32 s65, s68, 5
	s_add_i32 s65, s65, 0x21f50
	v_mov_b32_e32 v241, s65
	ds_read2_b32 v[236:237], v241 offset0:1 offset1:2
	ds_read2_b32 v[242:243], v241 offset0:3 offset1:4
	ds_read2_b32 v[244:245], v241 offset0:5 offset1:6
	ds_read_b32 v241, v241 offset:28
	s_waitcnt lgkmcnt(3)
	v_cmp_le_i32_e32 vcc, v236, v240
	s_nop 1
	v_cndmask_b32_e64 v236, 0, 1, vcc
	v_cmp_le_i32_e32 vcc, v237, v240
	s_nop 1
	v_cndmask_b32_e64 v237, 0, 1, vcc
	s_waitcnt lgkmcnt(2)
	v_cmp_le_i32_e32 vcc, v242, v240
	s_nop 1
	v_addc_co_u32_e32 v236, vcc, v237, v236, vcc
	v_cmp_le_i32_e32 vcc, v243, v240
	v_mov_b64_e32 v[242:243], s[8:9]
	s_nop 0
	v_cndmask_b32_e64 v237, 0, 1, vcc
	s_waitcnt lgkmcnt(1)
	v_cmp_le_i32_e32 vcc, v244, v240
	s_nop 1
	v_addc_co_u32_e32 v236, vcc, v236, v237, vcc
	v_cmp_le_i32_e32 vcc, v245, v240
	s_nop 1
	v_cndmask_b32_e64 v237, 0, 1, vcc
	s_waitcnt lgkmcnt(0)
	v_cmp_le_i32_e32 vcc, v241, v240
	s_nop 1
	v_addc_co_u32_e32 v246, vcc, v236, v237, vcc
	v_lshl_add_u32 v236, v246, 2, s65
	ds_read_b32 v241, v236
	v_mov_b32_e32 v247, 0
	v_lshlrev_b64 v[236:237], 8, v[246:247]
	v_lshl_add_u64 v[236:237], v[236:237], 0, s[68:69]
	v_mad_u64_u32 v[242:243], s[74:75], v236, s30, v[242:243]
	s_waitcnt lgkmcnt(0)
	v_sub_u32_e32 v240, v240, v241
	v_ashrrev_i32_e32 v241, 31, v240
	v_mad_i32_i24 v243, v237, s30, v243
	v_lshl_add_u64 v[236:237], v[240:241], 2, v[242:243]
	v_mov_b32_e32 v248, v236
	v_mov_b32_e32 v249, v237
	v_mov_b32_e32 v251, 1
.Lm2a_x_8:
	s_mov_b64 exec, s[70:71]
;     __device__ __forceinline__ void mainloop(bfr* smem, const AL& al, const BL& bl) {
;     ...
;         } else if constexpr (MI == 3) {
; #pragma unroll
;             for (int kt = 0; kt < nk; kt += 6) {
;                 G_STEP3(0, 1, sa0, sb0, 2, 2);
;                 G_STEP3(1, 2, sa1, sb1, 0, 2);
;                 G_STEP3(2, 0, sa0, sb0, 1, 2);
;                 G_STEP3(3, 1, sa1, sb1, 2, 2);
;                 G_STEP3(4, 2, sa0, sb0, 0, 2);
;                 G_STEP3(5, 0, sa1, sb1, 1, 2);
;             }
.Lm2a_ld_8:
	global_load_dword v234, v[248:249], off
	ds_read_b64_tr_b16 v[2:3], v232 offset:46096
	ds_read_b64_tr_b16 v[4:5], v232 offset:48400
	ds_read_b64_tr_b16 v[8:9], v232 offset:48464
	ds_read_b64_tr_b16 v[6:7], v232 offset:46160
	ds_read_b128 v[10:13], v219 offset:16
	ds_read_b128 v[146:149], v219 offset:48
	ds_read_b128 v[14:17], v219 offset:2576
	ds_read_b128 v[158:161], v219 offset:2608
	ds_read_b128 v[138:141], v219 offset:5136
	ds_read_b128 v[162:165], v219 offset:5168
	ds_read_b64_tr_b16 v[182:183], v232 offset:55312
	ds_read_b64_tr_b16 v[184:185], v232 offset:57616
	ds_read_b64_tr_b16 v[180:181], v232 offset:57680
	ds_read_b64_tr_b16 v[178:179], v232 offset:55376
	s_waitcnt lgkmcnt(9)
	v_mfma_f32_32x32x16_bf16 v[82:97], v[10:13], v[2:5], 0
	v_mfma_f32_32x32x16_bf16 v[66:81], v[10:13], v[6:9], 0
	ds_read_b128 v[166:169], v219 offset:15376
	s_waitcnt lgkmcnt(8)
	v_mfma_f32_32x32x16_bf16 v[50:65], v[14:17], v[2:5], 0
	v_mfma_f32_32x32x16_bf16 v[34:49], v[14:17], v[6:9], 0
	ds_read_b128 v[170:173], v219 offset:17936
	s_waitcnt lgkmcnt(7)
	v_mfma_f32_32x32x16_bf16 v[18:33], v[138:141], v[2:5], 0
	ds_read_b64_tr_b16 v[174:175], v220
	ds_read_b64_tr_b16 v[176:177], v220 offset:2304
	v_mfma_f32_32x32x16_bf16 v[2:17], v[138:141], v[6:9], 0
	ds_read_b128 v[138:141], v219 offset:20496
	ds_read_b64_tr_b16 v[154:155], v220 offset:64
	ds_read_b64_tr_b16 v[156:157], v220 offset:2368
	s_waitcnt lgkmcnt(9)
	v_mfma_f32_32x32x16_bf16 v[82:97], v[146:149], v[182:185], v[82:97]
	s_waitcnt vmcnt(10)
	ds_write_b128 v203, v[106:109] offset:30736
	s_and_saveexec_b64 s[12:13], s[4:5]
	ds_write_b128 v216, v[98:101] offset:40976
	s_or_b64 exec, exec, s[12:13]
	s_waitcnt lgkmcnt(8)
	v_mfma_f32_32x32x16_bf16 v[66:81], v[146:149], v[178:181], v[66:81]
	ds_read_b128 v[146:149], v219 offset:15408
	s_waitcnt vmcnt(9)
	v_cvt_pk_bf16_f32 v106, v134, v135
	v_cvt_pk_bf16_f32 v107, v136, v137
	s_waitcnt vmcnt(8)
	v_cvt_pk_bf16_f32 v108, v122, v123
	v_cvt_pk_bf16_f32 v109, v124, v125
	ds_write2_b64 v223, v[106:107], v[108:109] offset1:72
	s_waitcnt vmcnt(7)
	v_cvt_pk_bf16_f32 v106, v150, v151
	v_cvt_pk_bf16_f32 v107, v152, v153
	s_waitcnt vmcnt(6)
	v_cvt_pk_bf16_f32 v108, v142, v143
	v_cvt_pk_bf16_f32 v109, v144, v145
	ds_write2_b64 v223, v[106:107], v[108:109] offset0:144 offset1:216
	v_mfma_f32_32x32x16_bf16 v[50:65], v[158:161], v[182:185], v[50:65]
	global_load_dwordx4 v[106:109], v[200:201], off offset:256
	s_and_saveexec_b64 s[12:13], s[4:5]
	s_cbranch_execz .LBB0_1577
	global_load_dwordx4 v[98:101], v[206:207], off offset:256
.LBB0_1577:
	s_or_b64 exec, exec, s[12:13]
	v_add_co_u32_e32 v122, vcc, 0x80000, v214
	s_nop 1
	v_addc_co_u32_e32 v123, vcc, 0, v215, vcc
	v_add_co_u32_e32 v124, vcc, 0x81000, v214
	s_nop 1
	v_addc_co_u32_e32 v125, vcc, 0, v215, vcc
	v_add_co_u32_e32 v142, vcc, 0x82000, v214
	global_load_dwordx4 v[134:137], v[122:123], off
	s_nop 0
	global_load_dwordx4 v[122:125], v[124:125], off
	v_addc_co_u32_e32 v143, vcc, 0, v215, vcc
	v_add_co_u32_e32 v144, vcc, 0x83000, v214
	s_nop 1
	v_addc_co_u32_e32 v145, vcc, 0, v215, vcc
	global_load_dwordx4 v[150:153], v[142:143], off
	s_nop 0
	global_load_dwordx4 v[142:145], v[144:145], off
	v_mfma_f32_32x32x16_bf16 v[34:49], v[158:161], v[178:181], v[34:49]
	ds_read_b128 v[158:161], v219 offset:17968
	v_mfma_f32_32x32x16_bf16 v[18:33], v[162:165], v[182:185], v[18:33]
	ds_read_b64_tr_b16 v[182:183], v221
	ds_read_b64_tr_b16 v[184:185], v221 offset:2304
	v_mfma_f32_32x32x16_bf16 v[2:17], v[162:165], v[178:181], v[2:17]
	s_waitcnt lgkmcnt(10)
	v_mfma_f32_32x32x16_bf16 v[82:97], v[166:169], v[174:177], v[82:97]
	ds_read_b128 v[162:165], v219 offset:20528
	ds_read_b64_tr_b16 v[194:195], v222 offset:64
	ds_read_b64_tr_b16 v[196:197], v222 offset:2368
	s_waitcnt lgkmcnt(3)
	s_barrier
	v_mfma_f32_32x32x16_bf16 v[66:81], v[166:169], v[154:157], v[66:81]
	ds_read_b128 v[166:169], v219 offset:30736
	v_mfma_f32_32x32x16_bf16 v[50:65], v[170:173], v[174:177], v[50:65]
	v_mfma_f32_32x32x16_bf16 v[34:49], v[170:173], v[154:157], v[34:49]
	ds_read_b128 v[170:173], v219 offset:33296
	v_mfma_f32_32x32x16_bf16 v[18:33], v[138:141], v[174:177], v[18:33]
	ds_read_b64_tr_b16 v[178:179], v224
	ds_read_b64_tr_b16 v[180:181], v224 offset:2304
	v_mfma_f32_32x32x16_bf16 v[2:17], v[138:141], v[154:157], v[2:17]
	ds_read_b128 v[174:177], v219 offset:35856
	ds_read_b64_tr_b16 v[190:191], v224 offset:64
	ds_read_b64_tr_b16 v[192:193], v224 offset:2368
	v_mfma_f32_32x32x16_bf16 v[82:97], v[146:149], v[182:185], v[82:97]
	s_waitcnt vmcnt(10)
	ds_write_b128 v203, v[110:113] offset:16
	s_and_saveexec_b64 s[12:13], s[4:5]
	ds_write_b128 v216, v[102:105] offset:10256
	s_or_b64 exec, exec, s[12:13]
	s_waitcnt lgkmcnt(9)
	v_mfma_f32_32x32x16_bf16 v[66:81], v[146:149], v[194:197], v[66:81]
	ds_read_b128 v[110:113], v219 offset:30768
	s_waitcnt vmcnt(9)
	v_cvt_pk_bf16_f32 v118, v118, v119
	v_cvt_pk_bf16_f32 v119, v120, v121
	s_waitcnt vmcnt(8)
	v_cvt_pk_bf16_f32 v114, v114, v115
	v_cvt_pk_bf16_f32 v115, v116, v117
	ds_write2_b64 v198, v[118:119], v[114:115] offset0:130 offset1:202
	s_waitcnt vmcnt(7)
	v_cvt_pk_bf16_f32 v114, v130, v131
	v_cvt_pk_bf16_f32 v115, v132, v133
	s_waitcnt vmcnt(6)
	v_cvt_pk_bf16_f32 v116, v126, v127
	v_cvt_pk_bf16_f32 v117, v128, v129
	ds_write2_b64 v211, v[114:115], v[116:117] offset0:18 offset1:90
	v_mfma_f32_32x32x16_bf16 v[50:65], v[158:161], v[182:185], v[50:65]
	global_load_dwordx4 v[126:129], v[200:201], off offset:320
	s_and_saveexec_b64 s[12:13], s[4:5]
	s_cbranch_execz .LBB0_1581
	global_load_dwordx4 v[102:105], v[206:207], off offset:320

.LBB0_1589:
	s_or_b64 exec, exec, s[12:13]
	v_add_co_u32_e32 v130, vcc, 0xe0000, v214
	s_nop 1
	v_addc_co_u32_e32 v131, vcc, 0, v215, vcc
	v_add_co_u32_e32 v134, vcc, 0xe1000, v214
	s_nop 1
	v_addc_co_u32_e32 v135, vcc, 0, v215, vcc
	v_add_co_u32_e32 v138, vcc, 0xe2000, v214
	global_load_dwordx4 v[130:133], v[130:131], off
	s_nop 0
	global_load_dwordx4 v[134:137], v[134:135], off
	v_addc_co_u32_e32 v139, vcc, 0, v215, vcc
	v_add_co_u32_e32 v142, vcc, 0xe3000, v214
	s_nop 1
	v_addc_co_u32_e32 v143, vcc, 0, v215, vcc
	global_load_dwordx4 v[138:141], v[138:139], off
	s_nop 0
	global_load_dwordx4 v[142:145], v[142:143], off
	v_mfma_f32_32x32x16_bf16 v[34:49], v[158:161], v[194:197], v[34:49]
	ds_read_b128 v[146:149], v219 offset:17968
	v_mfma_f32_32x32x16_bf16 v[18:33], v[162:165], v[186:189], v[18:33]
	ds_read_b64_tr_b16 v[178:179], v221
	ds_read_b64_tr_b16 v[180:181], v221 offset:2304
	v_mfma_f32_32x32x16_bf16 v[2:17], v[162:165], v[194:197], v[2:17]
	s_waitcnt lgkmcnt(10)
	v_mfma_f32_32x32x16_bf16 v[82:97], v[166:169], v[182:185], v[82:97]
	ds_read_b128 v[154:157], v219 offset:20528
	ds_read_b64_tr_b16 v[194:195], v222 offset:64
	ds_read_b64_tr_b16 v[196:197], v222 offset:2368
	s_waitcnt lgkmcnt(3)
	s_barrier
	s_waitcnt vmcnt(15)
	v_cmp_ne_u32_e32 vcc, 0, v251
	s_nop 1
	v_cndmask_b32_e32 v250, v250, v234, vcc
	v_max_i32_e32 v236, 0, v250
	v_mov_b32_e32 v237, 0
	v_lshl_add_u64 v[236:237], v[236:237], 2, s[10:11]
	global_load_dword v235, v[236:237], off
	v_mfma_f32_32x32x16_bf16 v[66:81], v[166:169], v[190:193], v[66:81]
	ds_read_b128 v[158:161], v219 offset:30736
	v_mfma_f32_32x32x16_bf16 v[50:65], v[170:173], v[182:185], v[50:65]
	v_mfma_f32_32x32x16_bf16 v[34:49], v[170:173], v[190:193], v[34:49]
	ds_read_b128 v[162:165], v219 offset:33296
	v_mfma_f32_32x32x16_bf16 v[18:33], v[174:177], v[182:185], v[18:33]
	ds_read_b64_tr_b16 v[182:183], v224
	ds_read_b64_tr_b16 v[184:185], v224 offset:2304
	v_mfma_f32_32x32x16_bf16 v[2:17], v[174:177], v[190:193], v[2:17]
	ds_read_b128 v[166:169], v219 offset:35856
	ds_read_b64_tr_b16 v[186:187], v224 offset:64
	ds_read_b64_tr_b16 v[188:189], v224 offset:2368
	v_mfma_f32_32x32x16_bf16 v[82:97], v[150:153], v[178:181], v[82:97]
	s_waitcnt vmcnt(10)
	ds_write_b128 v203, v[106:109] offset:16
	s_and_saveexec_b64 s[12:13], s[4:5]
	ds_write_b128 v216, v[98:101] offset:10256
	s_or_b64 exec, exec, s[12:13]
	s_waitcnt lgkmcnt(9)
	v_mfma_f32_32x32x16_bf16 v[66:81], v[150:153], v[194:197], v[66:81]
	ds_read_b128 v[170:173], v219 offset:30768
	s_waitcnt vmcnt(9)
	v_cvt_pk_bf16_f32 v150, v118, v119
	v_cvt_pk_bf16_f32 v151, v120, v121
	s_waitcnt vmcnt(8)
	v_cvt_pk_bf16_f32 v152, v110, v111
	v_cvt_pk_bf16_f32 v153, v112, v113
	ds_write2_b64 v198, v[150:151], v[152:153] offset0:130 offset1:202
	s_waitcnt vmcnt(7)
	v_cvt_pk_bf16_f32 v150, v114, v115
	v_cvt_pk_bf16_f32 v151, v116, v117
	s_waitcnt vmcnt(6)
	v_cvt_pk_bf16_f32 v152, v122, v123
	v_cvt_pk_bf16_f32 v153, v124, v125
	ds_write2_b64 v211, v[150:151], v[152:153] offset0:18 offset1:90
	v_mfma_f32_32x32x16_bf16 v[50:65], v[146:149], v[178:181], v[50:65]
	v_mfma_f32_32x32x16_bf16 v[34:49], v[146:149], v[194:197], v[34:49]
	ds_read_b128 v[174:177], v219 offset:33328
	v_mfma_f32_32x32x16_bf16 v[18:33], v[154:157], v[178:181], v[18:33]
	ds_read_b64_tr_b16 v[178:179], v225
	ds_read_b64_tr_b16 v[180:181], v225 offset:2304
	v_mfma_f32_32x32x16_bf16 v[2:17], v[154:157], v[194:197], v[2:17]
	s_waitcnt lgkmcnt(10)
	v_mfma_f32_32x32x16_bf16 v[82:97], v[158:161], v[182:185], v[82:97]
	ds_read_b128 v[190:193], v219 offset:35888
	ds_read_b64_tr_b16 v[194:195], v226 offset:64
	ds_read_b64_tr_b16 v[196:197], v226 offset:2368
	s_waitcnt lgkmcnt(3)
	s_barrier
; __device__ __forceinline__ void phase_moe2(const Params& P, int layer, int tok0, int ntok, unsigned char* smraw, int bid, int nb) {
;     ...
;     while (u < nunits) {
;         gp.mainloop(smem, al, bl);
;         const int un = u + nrank;
;         if (un < nunits) { M2_SETUP(un, par ^ 1, epn); gp.prefetch(al, bl); }
	v_mfma_f32_32x32x16_bf16 v[66:81], v[158:161], v[186:189], v[66:81]
	ds_read_b128 v[154:157], v219 offset:16
	v_mfma_f32_32x32x16_bf16 v[50:65], v[162:165], v[182:185], v[50:65]
	v_mfma_f32_32x32x16_bf16 v[34:49], v[162:165], v[186:189], v[34:49]
	ds_read_b128 v[158:161], v219 offset:2576
	v_mfma_f32_32x32x16_bf16 v[18:33], v[166:169], v[182:185], v[18:33]
	ds_read_b64_tr_b16 v[162:163], v227 offset:46096
	ds_read_b64_tr_b16 v[164:165], v227 offset:48400
	v_mfma_f32_32x32x16_bf16 v[2:17], v[166:169], v[186:189], v[2:17]
	ds_read_b128 v[146:149], v219 offset:5136
	ds_read_b64_tr_b16 v[150:151], v227 offset:46160
	ds_read_b64_tr_b16 v[152:153], v227 offset:48464
	v_mfma_f32_32x32x16_bf16 v[82:97], v[170:173], v[178:181], v[82:97]
	s_waitcnt vmcnt(5)
	ds_write_b128 v203, v[126:129] offset:15376
	s_and_saveexec_b64 s[12:13], s[4:5]
	ds_write_b128 v216, v[102:105] offset:25616
	s_or_b64 exec, exec, s[12:13]
	s_waitcnt lgkmcnt(9)
	v_mfma_f32_32x32x16_bf16 v[66:81], v[170:173], v[194:197], v[66:81]
	ds_read_b128 v[166:169], v219 offset:48
	s_waitcnt vmcnt(4)
	v_cvt_pk_bf16_f32 v170, v130, v131
	v_cvt_pk_bf16_f32 v171, v132, v133
	s_waitcnt vmcnt(3)
	v_cvt_pk_bf16_f32 v172, v134, v135
	v_cvt_pk_bf16_f32 v173, v136, v137
	ds_write2_b64 v218, v[170:171], v[172:173] offset1:72
	s_waitcnt vmcnt(2)
	v_cvt_pk_bf16_f32 v170, v138, v139
	v_cvt_pk_bf16_f32 v171, v140, v141
	s_waitcnt vmcnt(1)
	v_cvt_pk_bf16_f32 v172, v142, v143
	v_cvt_pk_bf16_f32 v173, v144, v145
	ds_write2_b64 v218, v[170:171], v[172:173] offset0:144 offset1:216
	v_mfma_f32_32x32x16_bf16 v[50:65], v[174:177], v[178:181], v[50:65]
	v_mfma_f32_32x32x16_bf16 v[34:49], v[174:177], v[194:197], v[34:49]
	ds_read_b128 v[170:173], v219 offset:2608
	v_mfma_f32_32x32x16_bf16 v[18:33], v[190:193], v[178:181], v[18:33]
	ds_read_b64_tr_b16 v[174:175], v227 offset:55312
	ds_read_b64_tr_b16 v[176:177], v227 offset:57616
	v_mfma_f32_32x32x16_bf16 v[2:17], v[190:193], v[194:197], v[2:17]
	s_waitcnt lgkmcnt(10)
	v_mfma_f32_32x32x16_bf16 v[82:97], v[154:157], v[162:165], v[82:97]
	ds_read_b128 v[178:181], v219 offset:5168
	ds_read_b64_tr_b16 v[182:183], v227 offset:55376
	ds_read_b64_tr_b16 v[184:185], v227 offset:57680
	s_waitcnt lgkmcnt(3)
	s_barrier
	v_mfma_f32_32x32x16_bf16 v[66:81], v[154:157], v[150:153], v[66:81]
	ds_read_b128 v[154:157], v219 offset:15376
	v_mfma_f32_32x32x16_bf16 v[50:65], v[158:161], v[162:165], v[50:65]
	v_mfma_f32_32x32x16_bf16 v[34:49], v[158:161], v[150:153], v[34:49]
	ds_read_b128 v[158:161], v219 offset:17936
	v_mfma_f32_32x32x16_bf16 v[18:33], v[146:149], v[162:165], v[18:33]
	ds_read_b64_tr_b16 v[162:163], v220
	ds_read_b64_tr_b16 v[164:165], v220 offset:2304
	v_mfma_f32_32x32x16_bf16 v[2:17], v[146:149], v[150:153], v[2:17]
	ds_read_b128 v[146:149], v219 offset:20496
	ds_read_b64_tr_b16 v[150:151], v220 offset:64
	ds_read_b64_tr_b16 v[152:153], v220 offset:2368
	v_mfma_f32_32x32x16_bf16 v[82:97], v[166:169], v[174:177], v[82:97]
	s_waitcnt lgkmcnt(7)
	v_mfma_f32_32x32x16_bf16 v[66:81], v[166:169], v[182:185], v[66:81]
	ds_read_b128 v[166:169], v219 offset:15408
	v_mfma_f32_32x32x16_bf16 v[50:65], v[170:173], v[174:177], v[50:65]
	v_mfma_f32_32x32x16_bf16 v[34:49], v[170:173], v[182:185], v[34:49]
	ds_read_b128 v[170:173], v219 offset:17968
	v_mfma_f32_32x32x16_bf16 v[18:33], v[178:181], v[174:177], v[18:33]
	ds_read_b64_tr_b16 v[174:175], v221
	ds_read_b64_tr_b16 v[176:177], v221 offset:2304
	v_mfma_f32_32x32x16_bf16 v[2:17], v[178:181], v[182:185], v[2:17]
	s_waitcnt lgkmcnt(7)
	v_mfma_f32_32x32x16_bf16 v[82:97], v[154:157], v[162:165], v[82:97]
	ds_read_b128 v[178:181], v219 offset:20528
	ds_read_b64_tr_b16 v[182:183], v222 offset:64
	ds_read_b64_tr_b16 v[184:185], v222 offset:2368
	s_waitcnt lgkmcnt(3)
	s_barrier
	v_mfma_f32_32x32x16_bf16 v[66:81], v[154:157], v[150:153], v[66:81]
	v_mfma_f32_32x32x16_bf16 v[50:65], v[158:161], v[162:165], v[50:65]
	v_mfma_f32_32x32x16_bf16 v[34:49], v[158:161], v[150:153], v[34:49]
	v_mfma_f32_32x32x16_bf16 v[18:33], v[146:149], v[162:165], v[18:33]
	v_mfma_f32_32x32x16_bf16 v[2:17], v[146:149], v[150:153], v[2:17]
	v_mfma_f32_32x32x16_bf16 v[82:97], v[166:169], v[174:177], v[82:97]
	s_waitcnt lgkmcnt(0)
	v_mfma_f32_32x32x16_bf16 v[66:81], v[166:169], v[182:185], v[66:81]
	v_mfma_f32_32x32x16_bf16 v[50:65], v[170:173], v[174:177], v[50:65]
	v_mfma_f32_32x32x16_bf16 v[34:49], v[170:173], v[182:185], v[34:49]
	v_mfma_f32_32x32x16_bf16 v[18:33], v[178:181], v[174:177], v[18:33]
	v_mfma_f32_32x32x16_bf16 v[2:17], v[178:181], v[182:185], v[2:17]
	s_add_i32 s23, s23, s27
	s_cmp_ge_i32 s23, s24
	s_cselect_b64 s[12:13], -1, 0
	s_and_b64 vcc, exec, s[12:13]
	s_barrier
	s_cbranch_vccnz .LBB0_1614
	v_mov_b32_e32 v106, s29
	ds_read_b32 v106, v106
	s_ashr_i32 s0, s23, 2
	s_waitcnt lgkmcnt(0)
	v_cmp_ge_i32_e32 vcc, s0, v106
	s_cbranch_vccz .LBB0_1596
	v_sub_u32_e32 v106, s0, v106
	v_lshlrev_b32_e32 v106, 3, v106
	v_or_b32_e32 v108, s22, v106
	s_movk_i32 s14, 0x100
	s_cbranch_execz .LBB0_1597
	s_branch .LBB0_1600

; __device__ __forceinline__ int moe_row_pidx(const int* pre, const int* LIST, int e, int r) {
;     const int* pf = pre + 1360 + e * NREP;
;     int x = 0;
; #pragma unroll
;     for (int i = 1; i < NREP; ++i) x += (pf[i] <= r);
;     return LIST[((size_t)x * 256 + e) * LCAP + (r - pf[x])];
; }
.LBB0_1604:
	s_andn2_b64 vcc, exec, s[20:21]
	s_cbranch_vccnz .LBB0_1606
	s_lshl_b32 s0, s14, 5
	s_add_i32 s0, s0, 0
	s_add_i32 s0, s0, 0x21f50
	v_mov_b32_e32 v111, s0
	ds_read2_b32 v[106:107], v111 offset0:1 offset1:2
	ds_read2_b32 v[112:113], v111 offset0:3 offset1:4
	ds_read2_b32 v[114:115], v111 offset0:5 offset1:6
	ds_read_b32 v111, v111 offset:28
	s_waitcnt lgkmcnt(3)
	v_cmp_le_i32_e32 vcc, v106, v110
	s_nop 1
	v_cndmask_b32_e64 v106, 0, 1, vcc
	v_cmp_le_i32_e32 vcc, v107, v110
	s_nop 1
	v_cndmask_b32_e64 v107, 0, 1, vcc
	s_waitcnt lgkmcnt(2)
	v_cmp_le_i32_e32 vcc, v112, v110
	s_nop 1
	v_addc_co_u32_e32 v106, vcc, v107, v106, vcc
	v_cmp_le_i32_e32 vcc, v113, v110
	v_mov_b64_e32 v[112:113], s[8:9]
	s_nop 0
	v_cndmask_b32_e64 v107, 0, 1, vcc
	s_waitcnt lgkmcnt(1)
	v_cmp_le_i32_e32 vcc, v114, v110
	s_nop 1
	v_addc_co_u32_e32 v106, vcc, v106, v107, vcc
	v_cmp_le_i32_e32 vcc, v115, v110
	s_nop 1
	v_cndmask_b32_e64 v107, 0, 1, vcc
	s_waitcnt lgkmcnt(0)
	v_cmp_le_i32_e32 vcc, v111, v110
	s_nop 1
	v_addc_co_u32_e32 v198, vcc, v106, v107, vcc
	v_lshl_add_u32 v106, v198, 2, s0
	ds_read_b32 v111, v106
	v_lshlrev_b64 v[106:107], 8, v[198:199]
	v_lshl_add_u64 v[106:107], v[106:107], 0, s[14:15]
	v_mad_u64_u32 v[112:113], s[20:21], v106, s30, v[112:113]
	s_waitcnt lgkmcnt(0)
	v_sub_u32_e32 v110, v110, v111
	v_ashrrev_i32_e32 v111, 31, v110
	v_mad_i32_i24 v113, v107, s30, v113
	v_lshl_add_u64 v[106:107], v[110:111], 2, v[112:113]
	v_mov_b32_e32 v106, v234
.LBB0_1606:
	s_or_b64 exec, exec, s[18:19]
	v_lshl_add_u32 v107, v0, 2, s36
	s_waitcnt vmcnt(0)
	ds_write_b32 v107, v106
	v_cmp_lt_i32_e32 vcc, -1, v106
	v_mov_b32_e32 v107, 0
	s_and_saveexec_b64 s[18:19], vcc
	s_cbranch_execz .LBB0_1608
	v_mov_b32_e32 v107, v199
	v_lshl_add_u64 v[106:107], v[106:107], 2, s[10:11]
	v_mov_b32_e32 v107, v235

; __device__ __forceinline__ void moe_unit(const int* pre, const int* lpre, int x, int lb, int& e, int& rb) {
;     if (lb < lpre[32]) {
;         int lo = 0, hi = 32;
;         while (hi - lo > 1) { const int mid = (lo + hi) >> 1; if (lpre[mid] <= lb) lo = mid; else hi = mid; }
;         e = x + 8 * lo; rb = lb - lpre[lo];
;     } else { e = 256; rb = (lb - lpre[32]) * 8 + x; }
; }
.LBB0_2714:
	s_or_b64 exec, exec, s[12:13]
	v_add_co_u32_e32 v2, vcc, 0x60000, v212
	s_nop 1
	v_addc_co_u32_e32 v3, vcc, 0, v213, vcc
	v_add_co_u32_e32 v4, vcc, 0x61000, v212
	s_nop 1
	v_addc_co_u32_e32 v5, vcc, 0, v213, vcc
	global_load_dwordx4 v[118:121], v[2:3], off
	global_load_dwordx4 v[114:117], v[4:5], off
	v_add_co_u32_e32 v2, vcc, 0x62000, v212
	s_nop 1
	v_addc_co_u32_e32 v3, vcc, 0, v213, vcc
	v_add_co_u32_e32 v4, vcc, 0x63000, v212
	s_nop 1
	v_addc_co_u32_e32 v5, vcc, 0, v213, vcc
	global_load_dwordx4 v[130:133], v[2:3], off
	global_load_dwordx4 v[126:129], v[4:5], off
	s_waitcnt lgkmcnt(0)
	s_barrier
	s_add_i32 s64, s23, s27
	v_mov_b64_e32 v[248:249], s[8:9]
	v_mov_b32_e32 v250, -1
	v_mov_b32_e32 v251, 0
	s_cmp_ge_i32 s64, s24
	s_cbranch_scc1 .Lm2a_ld_18
	v_mov_b32_e32 v236, s31
	ds_read_b32 v236, v236
	s_ashr_i32 s65, s64, 2
	s_waitcnt lgkmcnt(0)
	v_cmp_ge_i32_e32 vcc, s65, v236
	s_cbranch_vccz .Lm2a_rt_18
	v_sub_u32_e32 v236, s65, v236
	v_lshlrev_b32_e32 v236, 3, v236
	v_or_b32_e32 v238, s22, v236
	s_movk_i32 s68, 0x100
	s_branch .Lm2a_have_18

; __device__ __forceinline__ int moe_row_pidx(const int* pre, const int* LIST, int e, int r) {
;     const int* pf = pre + 1360 + e * NREP;
;     int x = 0;
; #pragma unroll
;     for (int i = 1; i < NREP; ++i) x += (pf[i] <= r);
;     return LIST[((size_t)x * 256 + e) * LCAP + (r - pf[x])];
; }
.Lm2a_rt2_18:
	s_lshl_b32 s65, s68, 5
	s_add_i32 s65, s65, 0x21f50
	v_mov_b32_e32 v241, s65
	ds_read2_b32 v[236:237], v241 offset0:1 offset1:2
	ds_read2_b32 v[242:243], v241 offset0:3 offset1:4
	ds_read2_b32 v[244:245], v241 offset0:5 offset1:6
	ds_read_b32 v241, v241 offset:28
	s_waitcnt lgkmcnt(3)
	v_cmp_le_i32_e32 vcc, v236, v240
	s_nop 1
	v_cndmask_b32_e64 v236, 0, 1, vcc
	v_cmp_le_i32_e32 vcc, v237, v240
	s_nop 1
	v_cndmask_b32_e64 v237, 0, 1, vcc
	s_waitcnt lgkmcnt(2)
	v_cmp_le_i32_e32 vcc, v242, v240
	s_nop 1
	v_addc_co_u32_e32 v236, vcc, v237, v236, vcc
	v_cmp_le_i32_e32 vcc, v243, v240
	v_mov_b64_e32 v[242:243], s[8:9]
	s_nop 0
	v_cndmask_b32_e64 v237, 0, 1, vcc
	s_waitcnt lgkmcnt(1)
	v_cmp_le_i32_e32 vcc, v244, v240
	s_nop 1
	v_addc_co_u32_e32 v236, vcc, v236, v237, vcc
	v_cmp_le_i32_e32 vcc, v245, v240
	s_nop 1
	v_cndmask_b32_e64 v237, 0, 1, vcc
	s_waitcnt lgkmcnt(0)
	v_cmp_le_i32_e32 vcc, v241, v240
	s_nop 1
	v_addc_co_u32_e32 v246, vcc, v236, v237, vcc
	v_lshl_add_u32 v236, v246, 2, s65
	ds_read_b32 v241, v236
	v_mov_b32_e32 v247, 0
	v_lshlrev_b64 v[236:237], 8, v[246:247]
	v_lshl_add_u64 v[236:237], v[236:237], 0, s[68:69]
	v_mad_u64_u32 v[242:243], s[74:75], v236, s34, v[242:243]
	s_waitcnt lgkmcnt(0)
	v_sub_u32_e32 v240, v240, v241
	v_ashrrev_i32_e32 v241, 31, v240
	v_mad_i32_i24 v243, v237, s34, v243
	v_lshl_add_u64 v[236:237], v[240:241], 2, v[242:243]
	v_mov_b32_e32 v248, v236
	v_mov_b32_e32 v249, v237
	v_mov_b32_e32 v251, 1

;     __device__ __forceinline__ void mainloop(bfr* smem, const AL& al, const BL& bl) {
;     ...
;         } else if constexpr (MI == 3) {
; #pragma unroll
;             for (int kt = 0; kt < nk; kt += 6) {
;                 G_STEP3(0, 1, sa0, sb0, 2, 2);
;                 G_STEP3(1, 2, sa1, sb1, 0, 2);
;                 G_STEP3(2, 0, sa0, sb0, 1, 2);
;                 G_STEP3(3, 1, sa1, sb1, 2, 2);
;                 G_STEP3(4, 2, sa0, sb0, 0, 2);
;                 G_STEP3(5, 0, sa1, sb1, 1, 2);
;             }
.Lm2a_ld_18:
	global_load_dword v234, v[248:249], off
	ds_read_b64_tr_b16 v[2:3], v231 offset:46096
	ds_read_b64_tr_b16 v[4:5], v231 offset:48400
	ds_read_b64_tr_b16 v[8:9], v231 offset:48464
	ds_read_b64_tr_b16 v[6:7], v231 offset:46160
	ds_read_b128 v[10:13], v218 offset:16
	ds_read_b128 v[146:149], v218 offset:48
	ds_read_b128 v[14:17], v218 offset:2576
	ds_read_b128 v[158:161], v218 offset:2608
	ds_read_b128 v[138:141], v218 offset:5136
	ds_read_b128 v[162:165], v218 offset:5168
	ds_read_b64_tr_b16 v[182:183], v231 offset:55312
	ds_read_b64_tr_b16 v[184:185], v231 offset:57616
	ds_read_b64_tr_b16 v[180:181], v231 offset:57680
	ds_read_b64_tr_b16 v[178:179], v231 offset:55376
	s_waitcnt lgkmcnt(9)
	v_mfma_f32_32x32x16_bf16 v[82:97], v[10:13], v[2:5], 0
	v_mfma_f32_32x32x16_bf16 v[66:81], v[10:13], v[6:9], 0
	ds_read_b128 v[166:169], v218 offset:15376
	s_waitcnt lgkmcnt(8)
	v_mfma_f32_32x32x16_bf16 v[50:65], v[14:17], v[2:5], 0
	v_mfma_f32_32x32x16_bf16 v[34:49], v[14:17], v[6:9], 0
	ds_read_b128 v[170:173], v218 offset:17936
	s_waitcnt lgkmcnt(7)
	v_mfma_f32_32x32x16_bf16 v[18:33], v[138:141], v[2:5], 0
	ds_read_b64_tr_b16 v[174:175], v219
	ds_read_b64_tr_b16 v[176:177], v219 offset:2304
	v_mfma_f32_32x32x16_bf16 v[2:17], v[138:141], v[6:9], 0
	ds_read_b128 v[138:141], v218 offset:20496
	ds_read_b64_tr_b16 v[154:155], v219 offset:64
	ds_read_b64_tr_b16 v[156:157], v219 offset:2368
	s_waitcnt lgkmcnt(9)
	v_mfma_f32_32x32x16_bf16 v[82:97], v[146:149], v[182:185], v[82:97]
	s_waitcnt vmcnt(10)
	ds_write_b128 v214, v[106:109] offset:30736
	s_and_saveexec_b64 s[12:13], s[4:5]
	ds_write_b128 v215, v[98:101] offset:40976
	s_or_b64 exec, exec, s[12:13]
	s_waitcnt lgkmcnt(8)
	v_mfma_f32_32x32x16_bf16 v[66:81], v[146:149], v[178:181], v[66:81]
	ds_read_b128 v[146:149], v218 offset:15408
	s_waitcnt vmcnt(9)
	v_cvt_pk_bf16_f32 v106, v134, v135
	v_cvt_pk_bf16_f32 v107, v136, v137
	s_waitcnt vmcnt(8)
	v_cvt_pk_bf16_f32 v108, v122, v123
	v_cvt_pk_bf16_f32 v109, v124, v125
	ds_write2_b64 v222, v[106:107], v[108:109] offset1:72
	s_waitcnt vmcnt(7)
	v_cvt_pk_bf16_f32 v106, v150, v151
	v_cvt_pk_bf16_f32 v107, v152, v153
	s_waitcnt vmcnt(6)
	v_cvt_pk_bf16_f32 v108, v142, v143
	v_cvt_pk_bf16_f32 v109, v144, v145
	ds_write2_b64 v222, v[106:107], v[108:109] offset0:144 offset1:216
	v_mfma_f32_32x32x16_bf16 v[50:65], v[158:161], v[182:185], v[50:65]
	global_load_dwordx4 v[106:109], v[200:201], off offset:256
	s_and_saveexec_b64 s[12:13], s[4:5]
	s_cbranch_execz .LBB0_2718
	global_load_dwordx4 v[98:101], v[202:203], off offset:256
.LBB0_2718:
	s_or_b64 exec, exec, s[12:13]
	v_add_co_u32_e32 v122, vcc, 0x80000, v212
	s_nop 1
	v_addc_co_u32_e32 v123, vcc, 0, v213, vcc
	v_add_co_u32_e32 v124, vcc, 0x81000, v212
	s_nop 1
	v_addc_co_u32_e32 v125, vcc, 0, v213, vcc
	v_add_co_u32_e32 v142, vcc, 0x82000, v212
	global_load_dwordx4 v[134:137], v[122:123], off
	s_nop 0
	global_load_dwordx4 v[122:125], v[124:125], off
	v_addc_co_u32_e32 v143, vcc, 0, v213, vcc
	v_add_co_u32_e32 v144, vcc, 0x83000, v212
	s_nop 1
	v_addc_co_u32_e32 v145, vcc, 0, v213, vcc
	global_load_dwordx4 v[150:153], v[142:143], off
	s_nop 0
	global_load_dwordx4 v[142:145], v[144:145], off
	v_mfma_f32_32x32x16_bf16 v[34:49], v[158:161], v[178:181], v[34:49]
	ds_read_b128 v[158:161], v218 offset:17968
	v_mfma_f32_32x32x16_bf16 v[18:33], v[162:165], v[182:185], v[18:33]
	ds_read_b64_tr_b16 v[182:183], v220
	ds_read_b64_tr_b16 v[184:185], v220 offset:2304
	v_mfma_f32_32x32x16_bf16 v[2:17], v[162:165], v[178:181], v[2:17]
	s_waitcnt lgkmcnt(10)
	v_mfma_f32_32x32x16_bf16 v[82:97], v[166:169], v[174:177], v[82:97]
	ds_read_b128 v[162:165], v218 offset:20528
	ds_read_b64_tr_b16 v[194:195], v221 offset:64
	ds_read_b64_tr_b16 v[196:197], v221 offset:2368
	s_waitcnt lgkmcnt(3)
	s_barrier
	v_mfma_f32_32x32x16_bf16 v[66:81], v[166:169], v[154:157], v[66:81]
	ds_read_b128 v[166:169], v218 offset:30736
	v_mfma_f32_32x32x16_bf16 v[50:65], v[170:173], v[174:177], v[50:65]
	v_mfma_f32_32x32x16_bf16 v[34:49], v[170:173], v[154:157], v[34:49]
	ds_read_b128 v[170:173], v218 offset:33296
	v_mfma_f32_32x32x16_bf16 v[18:33], v[138:141], v[174:177], v[18:33]
	ds_read_b64_tr_b16 v[178:179], v223
	ds_read_b64_tr_b16 v[180:181], v223 offset:2304
	v_mfma_f32_32x32x16_bf16 v[2:17], v[138:141], v[154:157], v[2:17]
	ds_read_b128 v[174:177], v218 offset:35856
	ds_read_b64_tr_b16 v[190:191], v223 offset:64
	ds_read_b64_tr_b16 v[192:193], v223 offset:2368
	v_mfma_f32_32x32x16_bf16 v[82:97], v[146:149], v[182:185], v[82:97]
	s_waitcnt vmcnt(10)
	ds_write_b128 v214, v[110:113] offset:16
	s_and_saveexec_b64 s[12:13], s[4:5]
	ds_write_b128 v215, v[102:105] offset:10256
	s_or_b64 exec, exec, s[12:13]
	s_waitcnt lgkmcnt(9)
	v_mfma_f32_32x32x16_bf16 v[66:81], v[146:149], v[194:197], v[66:81]
	ds_read_b128 v[110:113], v218 offset:30768
	s_waitcnt vmcnt(9)
	v_cvt_pk_bf16_f32 v118, v118, v119
	v_cvt_pk_bf16_f32 v119, v120, v121
	s_waitcnt vmcnt(8)
	v_cvt_pk_bf16_f32 v114, v114, v115
	v_cvt_pk_bf16_f32 v115, v116, v117
	ds_write2_b64 v198, v[118:119], v[114:115] offset0:130 offset1:202
	s_waitcnt vmcnt(7)
	v_cvt_pk_bf16_f32 v114, v130, v131
	v_cvt_pk_bf16_f32 v115, v132, v133
	s_waitcnt vmcnt(6)
	v_cvt_pk_bf16_f32 v116, v126, v127
	v_cvt_pk_bf16_f32 v117, v128, v129
	ds_write2_b64 v209, v[114:115], v[116:117] offset0:18 offset1:90
	v_mfma_f32_32x32x16_bf16 v[50:65], v[158:161], v[182:185], v[50:65]
	global_load_dwordx4 v[126:129], v[200:201], off offset:320
	s_and_saveexec_b64 s[12:13], s[4:5]
	s_cbranch_execz .LBB0_2722
	global_load_dwordx4 v[102:105], v[202:203], off offset:320

.LBB0_2730:
	s_or_b64 exec, exec, s[12:13]
	v_add_co_u32_e32 v130, vcc, 0xe0000, v212
	s_nop 1
	v_addc_co_u32_e32 v131, vcc, 0, v213, vcc
	v_add_co_u32_e32 v134, vcc, 0xe1000, v212
	s_nop 1
	v_addc_co_u32_e32 v135, vcc, 0, v213, vcc
	v_add_co_u32_e32 v138, vcc, 0xe2000, v212
	global_load_dwordx4 v[130:133], v[130:131], off
	s_nop 0
	global_load_dwordx4 v[134:137], v[134:135], off
	v_addc_co_u32_e32 v139, vcc, 0, v213, vcc
	v_add_co_u32_e32 v142, vcc, 0xe3000, v212
	s_nop 1
	v_addc_co_u32_e32 v143, vcc, 0, v213, vcc
	global_load_dwordx4 v[138:141], v[138:139], off
	s_nop 0
	global_load_dwordx4 v[142:145], v[142:143], off
	v_mfma_f32_32x32x16_bf16 v[34:49], v[158:161], v[194:197], v[34:49]
	ds_read_b128 v[146:149], v218 offset:17968
	v_mfma_f32_32x32x16_bf16 v[18:33], v[162:165], v[186:189], v[18:33]
	ds_read_b64_tr_b16 v[178:179], v220
	ds_read_b64_tr_b16 v[180:181], v220 offset:2304
	v_mfma_f32_32x32x16_bf16 v[2:17], v[162:165], v[194:197], v[2:17]
	s_waitcnt lgkmcnt(10)
	v_mfma_f32_32x32x16_bf16 v[82:97], v[166:169], v[182:185], v[82:97]
	ds_read_b128 v[154:157], v218 offset:20528
	ds_read_b64_tr_b16 v[194:195], v221 offset:64
	ds_read_b64_tr_b16 v[196:197], v221 offset:2368
	s_waitcnt lgkmcnt(3)
	s_barrier
	s_waitcnt vmcnt(15)
	v_cmp_ne_u32_e32 vcc, 0, v251
	s_nop 1
	v_cndmask_b32_e32 v250, v250, v234, vcc
	v_max_i32_e32 v236, 0, v250
	v_mov_b32_e32 v237, 0
	v_lshl_add_u64 v[236:237], v[236:237], 2, s[10:11]
	global_load_dword v235, v[236:237], off
	v_mfma_f32_32x32x16_bf16 v[66:81], v[166:169], v[190:193], v[66:81]
	ds_read_b128 v[158:161], v218 offset:30736
	v_mfma_f32_32x32x16_bf16 v[50:65], v[170:173], v[182:185], v[50:65]
	v_mfma_f32_32x32x16_bf16 v[34:49], v[170:173], v[190:193], v[34:49]
	ds_read_b128 v[162:165], v218 offset:33296
	v_mfma_f32_32x32x16_bf16 v[18:33], v[174:177], v[182:185], v[18:33]
	ds_read_b64_tr_b16 v[182:183], v223
	ds_read_b64_tr_b16 v[184:185], v223 offset:2304
	v_mfma_f32_32x32x16_bf16 v[2:17], v[174:177], v[190:193], v[2:17]
	ds_read_b128 v[166:169], v218 offset:35856
	ds_read_b64_tr_b16 v[186:187], v223 offset:64
	ds_read_b64_tr_b16 v[188:189], v223 offset:2368
	v_mfma_f32_32x32x16_bf16 v[82:97], v[150:153], v[178:181], v[82:97]
	s_waitcnt vmcnt(10)
	ds_write_b128 v214, v[106:109] offset:16
	s_and_saveexec_b64 s[12:13], s[4:5]
	ds_write_b128 v215, v[98:101] offset:10256
	s_or_b64 exec, exec, s[12:13]
	s_waitcnt lgkmcnt(9)
	v_mfma_f32_32x32x16_bf16 v[66:81], v[150:153], v[194:197], v[66:81]
	ds_read_b128 v[170:173], v218 offset:30768
	s_waitcnt vmcnt(9)
	v_cvt_pk_bf16_f32 v150, v118, v119
	v_cvt_pk_bf16_f32 v151, v120, v121
	s_waitcnt vmcnt(8)
	v_cvt_pk_bf16_f32 v152, v110, v111
	v_cvt_pk_bf16_f32 v153, v112, v113
	ds_write2_b64 v198, v[150:151], v[152:153] offset0:130 offset1:202
	s_waitcnt vmcnt(7)
	v_cvt_pk_bf16_f32 v150, v114, v115
	v_cvt_pk_bf16_f32 v151, v116, v117
	s_waitcnt vmcnt(6)
	v_cvt_pk_bf16_f32 v152, v122, v123
	v_cvt_pk_bf16_f32 v153, v124, v125
	ds_write2_b64 v209, v[150:151], v[152:153] offset0:18 offset1:90
	v_mfma_f32_32x32x16_bf16 v[50:65], v[146:149], v[178:181], v[50:65]
	v_mfma_f32_32x32x16_bf16 v[34:49], v[146:149], v[194:197], v[34:49]
	ds_read_b128 v[174:177], v218 offset:33328
	v_mfma_f32_32x32x16_bf16 v[18:33], v[154:157], v[178:181], v[18:33]
	ds_read_b64_tr_b16 v[178:179], v224
	ds_read_b64_tr_b16 v[180:181], v224 offset:2304
	v_mfma_f32_32x32x16_bf16 v[2:17], v[154:157], v[194:197], v[2:17]
	s_waitcnt lgkmcnt(10)
	v_mfma_f32_32x32x16_bf16 v[82:97], v[158:161], v[182:185], v[82:97]
	ds_read_b128 v[190:193], v218 offset:35888
	ds_read_b64_tr_b16 v[194:195], v225 offset:64
	ds_read_b64_tr_b16 v[196:197], v225 offset:2368
	s_waitcnt lgkmcnt(3)
	s_barrier
; __device__ __forceinline__ void phase_moe2(const Params& P, int layer, int tok0, int ntok, unsigned char* smraw, int bid, int nb) {
;     ...
;     while (u < nunits) {
;         gp.mainloop(smem, al, bl);
;         const int un = u + nrank;
;         if (un < nunits) { M2_SETUP(un, par ^ 1, epn); gp.prefetch(al, bl); }
	v_mfma_f32_32x32x16_bf16 v[66:81], v[158:161], v[186:189], v[66:81]
	ds_read_b128 v[154:157], v218 offset:16
	v_mfma_f32_32x32x16_bf16 v[50:65], v[162:165], v[182:185], v[50:65]
	v_mfma_f32_32x32x16_bf16 v[34:49], v[162:165], v[186:189], v[34:49]
	ds_read_b128 v[158:161], v218 offset:2576
	v_mfma_f32_32x32x16_bf16 v[18:33], v[166:169], v[182:185], v[18:33]
	ds_read_b64_tr_b16 v[162:163], v226 offset:46096
	ds_read_b64_tr_b16 v[164:165], v226 offset:48400
	v_mfma_f32_32x32x16_bf16 v[2:17], v[166:169], v[186:189], v[2:17]
	ds_read_b128 v[146:149], v218 offset:5136
	ds_read_b64_tr_b16 v[150:151], v226 offset:46160
	ds_read_b64_tr_b16 v[152:153], v226 offset:48464
	v_mfma_f32_32x32x16_bf16 v[82:97], v[170:173], v[178:181], v[82:97]
	s_waitcnt vmcnt(5)
	ds_write_b128 v214, v[126:129] offset:15376
	s_and_saveexec_b64 s[12:13], s[4:5]
	ds_write_b128 v215, v[102:105] offset:25616
	s_or_b64 exec, exec, s[12:13]
	s_waitcnt lgkmcnt(9)
	v_mfma_f32_32x32x16_bf16 v[66:81], v[170:173], v[194:197], v[66:81]
	ds_read_b128 v[166:169], v218 offset:48
	s_waitcnt vmcnt(4)
	v_cvt_pk_bf16_f32 v170, v130, v131
	v_cvt_pk_bf16_f32 v171, v132, v133
	s_waitcnt vmcnt(3)
	v_cvt_pk_bf16_f32 v172, v134, v135
	v_cvt_pk_bf16_f32 v173, v136, v137
	ds_write2_b64 v217, v[170:171], v[172:173] offset1:72
	s_waitcnt vmcnt(2)
	v_cvt_pk_bf16_f32 v170, v138, v139
	v_cvt_pk_bf16_f32 v171, v140, v141
	s_waitcnt vmcnt(1)
	v_cvt_pk_bf16_f32 v172, v142, v143
	v_cvt_pk_bf16_f32 v173, v144, v145
	ds_write2_b64 v217, v[170:171], v[172:173] offset0:144 offset1:216
	v_mfma_f32_32x32x16_bf16 v[50:65], v[174:177], v[178:181], v[50:65]
	v_mfma_f32_32x32x16_bf16 v[34:49], v[174:177], v[194:197], v[34:49]
	ds_read_b128 v[170:173], v218 offset:2608
	v_mfma_f32_32x32x16_bf16 v[18:33], v[190:193], v[178:181], v[18:33]
	ds_read_b64_tr_b16 v[174:175], v226 offset:55312
	ds_read_b64_tr_b16 v[176:177], v226 offset:57616
	v_mfma_f32_32x32x16_bf16 v[2:17], v[190:193], v[194:197], v[2:17]
	s_waitcnt lgkmcnt(10)
	v_mfma_f32_32x32x16_bf16 v[82:97], v[154:157], v[162:165], v[82:97]
	ds_read_b128 v[178:181], v218 offset:5168
	ds_read_b64_tr_b16 v[182:183], v226 offset:55376
	ds_read_b64_tr_b16 v[184:185], v226 offset:57680
	s_waitcnt lgkmcnt(3)
	s_barrier
	v_mfma_f32_32x32x16_bf16 v[66:81], v[154:157], v[150:153], v[66:81]
	ds_read_b128 v[154:157], v218 offset:15376
	v_mfma_f32_32x32x16_bf16 v[50:65], v[158:161], v[162:165], v[50:65]
	v_mfma_f32_32x32x16_bf16 v[34:49], v[158:161], v[150:153], v[34:49]
	ds_read_b128 v[158:161], v218 offset:17936
	v_mfma_f32_32x32x16_bf16 v[18:33], v[146:149], v[162:165], v[18:33]
	ds_read_b64_tr_b16 v[162:163], v219
	ds_read_b64_tr_b16 v[164:165], v219 offset:2304
	v_mfma_f32_32x32x16_bf16 v[2:17], v[146:149], v[150:153], v[2:17]
	ds_read_b128 v[146:149], v218 offset:20496
	ds_read_b64_tr_b16 v[150:151], v219 offset:64
	ds_read_b64_tr_b16 v[152:153], v219 offset:2368
	v_mfma_f32_32x32x16_bf16 v[82:97], v[166:169], v[174:177], v[82:97]
	s_waitcnt lgkmcnt(7)
	v_mfma_f32_32x32x16_bf16 v[66:81], v[166:169], v[182:185], v[66:81]
	ds_read_b128 v[166:169], v218 offset:15408
	v_mfma_f32_32x32x16_bf16 v[50:65], v[170:173], v[174:177], v[50:65]
	v_mfma_f32_32x32x16_bf16 v[34:49], v[170:173], v[182:185], v[34:49]
	ds_read_b128 v[170:173], v218 offset:17968
	v_mfma_f32_32x32x16_bf16 v[18:33], v[178:181], v[174:177], v[18:33]
	ds_read_b64_tr_b16 v[174:175], v220
	ds_read_b64_tr_b16 v[176:177], v220 offset:2304
	v_mfma_f32_32x32x16_bf16 v[2:17], v[178:181], v[182:185], v[2:17]
	s_waitcnt lgkmcnt(7)
	v_mfma_f32_32x32x16_bf16 v[82:97], v[154:157], v[162:165], v[82:97]
	ds_read_b128 v[178:181], v218 offset:20528
	ds_read_b64_tr_b16 v[182:183], v221 offset:64
	ds_read_b64_tr_b16 v[184:185], v221 offset:2368
	s_waitcnt lgkmcnt(3)
	s_barrier
	v_mfma_f32_32x32x16_bf16 v[66:81], v[154:157], v[150:153], v[66:81]
	v_mfma_f32_32x32x16_bf16 v[50:65], v[158:161], v[162:165], v[50:65]
	v_mfma_f32_32x32x16_bf16 v[34:49], v[158:161], v[150:153], v[34:49]
	v_mfma_f32_32x32x16_bf16 v[18:33], v[146:149], v[162:165], v[18:33]
	v_mfma_f32_32x32x16_bf16 v[2:17], v[146:149], v[150:153], v[2:17]
	v_mfma_f32_32x32x16_bf16 v[82:97], v[166:169], v[174:177], v[82:97]
	s_waitcnt lgkmcnt(0)
	v_mfma_f32_32x32x16_bf16 v[66:81], v[166:169], v[182:185], v[66:81]
	v_mfma_f32_32x32x16_bf16 v[50:65], v[170:173], v[174:177], v[50:65]
	v_mfma_f32_32x32x16_bf16 v[34:49], v[170:173], v[182:185], v[34:49]
	v_mfma_f32_32x32x16_bf16 v[18:33], v[178:181], v[174:177], v[18:33]
	v_mfma_f32_32x32x16_bf16 v[2:17], v[178:181], v[182:185], v[2:17]
	s_add_i32 s23, s23, s27
	s_cmp_ge_i32 s23, s24
	s_cselect_b64 s[12:13], -1, 0
	s_and_b64 vcc, exec, s[12:13]
	s_barrier
	s_cbranch_vccnz .LBB0_2755
	v_mov_b32_e32 v106, s31
	ds_read_b32 v106, v106
	s_ashr_i32 s0, s23, 2
	s_waitcnt lgkmcnt(0)
	v_cmp_ge_i32_e32 vcc, s0, v106
	s_cbranch_vccz .LBB0_2737
	v_sub_u32_e32 v106, s0, v106
	v_lshlrev_b32_e32 v106, 3, v106
	v_or_b32_e32 v108, s22, v106
	s_movk_i32 s14, 0x100
	s_cbranch_execz .LBB0_2738
	s_branch .LBB0_2741

; __device__ __forceinline__ int moe_row_pidx(const int* pre, const int* LIST, int e, int r) {
;     const int* pf = pre + 1360 + e * NREP;
;     int x = 0;
; #pragma unroll
;     for (int i = 1; i < NREP; ++i) x += (pf[i] <= r);
;     return LIST[((size_t)x * 256 + e) * LCAP + (r - pf[x])];
; }
.LBB0_2745:
	s_andn2_b64 vcc, exec, s[20:21]
	s_cbranch_vccnz .LBB0_2747
	s_lshl_b32 s0, s14, 5
	s_add_i32 s0, s0, 0
	s_add_i32 s0, s0, 0x21f50
	v_mov_b32_e32 v111, s0
	ds_read2_b32 v[106:107], v111 offset0:1 offset1:2
	ds_read2_b32 v[112:113], v111 offset0:3 offset1:4
	ds_read2_b32 v[114:115], v111 offset0:5 offset1:6
	ds_read_b32 v111, v111 offset:28
	s_waitcnt lgkmcnt(3)
	v_cmp_le_i32_e32 vcc, v106, v110
	s_nop 1
	v_cndmask_b32_e64 v106, 0, 1, vcc
	v_cmp_le_i32_e32 vcc, v107, v110
	s_nop 1
	v_cndmask_b32_e64 v107, 0, 1, vcc
	s_waitcnt lgkmcnt(2)
	v_cmp_le_i32_e32 vcc, v112, v110
	s_nop 1
	v_addc_co_u32_e32 v106, vcc, v107, v106, vcc
	v_cmp_le_i32_e32 vcc, v113, v110
	v_mov_b64_e32 v[112:113], s[8:9]
	s_nop 0
	v_cndmask_b32_e64 v107, 0, 1, vcc
	s_waitcnt lgkmcnt(1)
	v_cmp_le_i32_e32 vcc, v114, v110
	s_nop 1
	v_addc_co_u32_e32 v106, vcc, v106, v107, vcc
	v_cmp_le_i32_e32 vcc, v115, v110
	s_nop 1
	v_cndmask_b32_e64 v107, 0, 1, vcc
	s_waitcnt lgkmcnt(0)
	v_cmp_le_i32_e32 vcc, v111, v110
	s_nop 1
	v_addc_co_u32_e32 v198, vcc, v106, v107, vcc
	v_lshl_add_u32 v106, v198, 2, s0
	ds_read_b32 v111, v106
	v_lshlrev_b64 v[106:107], 8, v[198:199]
	v_lshl_add_u64 v[106:107], v[106:107], 0, s[14:15]
	v_mad_u64_u32 v[112:113], s[20:21], v106, s34, v[112:113]
	s_waitcnt lgkmcnt(0)
	v_sub_u32_e32 v110, v110, v111
	v_ashrrev_i32_e32 v111, 31, v110
	v_mad_i32_i24 v113, v107, s34, v113
	v_lshl_add_u64 v[106:107], v[110:111], 2, v[112:113]
	v_mov_b32_e32 v106, v234
.LBB0_2747:
	s_or_b64 exec, exec, s[18:19]
	v_lshl_add_u32 v107, v0, 2, s38
	s_waitcnt vmcnt(0)
	ds_write_b32 v107, v106
	v_cmp_lt_i32_e32 vcc, -1, v106
	v_mov_b32_e32 v107, 0
	s_and_saveexec_b64 s[18:19], vcc
	s_cbranch_execz .LBB0_2749
	v_mov_b32_e32 v107, v199
	v_lshl_add_u64 v[106:107], v[106:107], 2, s[10:11]
	v_mov_b32_e32 v107, v235
